# four-waves-per-row scanner with the per-row constants hoisted out of the row loop (row parity is constant) and the buffer flag read one row ahead
# speedup vs baseline: 1.0238x; 1.0238x over previous
.LBB1_217:
	s_andn2_saveexec_b64 s[0:1], s[30:31]
	s_cbranch_execz .LBB1_384
	v_readfirstlane_b32 s34, v1
	v_readfirstlane_b32 s36, v84
	v_and_b32_e32 v3, 63, v0
	v_lshlrev_b32_e32 v2, 4, v3
	s_cmp_lt_i32 s36, 0
	s_cbranch_scc1 .LBB1_384
	s_add_i32 s36, s36, 1
	s_lshl_b32 s36, s36, 2
	s_sub_i32 s36, s36, 1
	s_lshr_b32 s33, s33, 2
	s_mov_b32 s55, s34
	s_mul_i32 s43, s55, 0x2800
	s_and_b32 s56, s2, 7
	s_lshr_b32 s57, s2, 3
	s_mul_i32 s37, s56, 31
	s_min_u32 s56, s56, 2
	s_add_u32 s37, s37, s56
	s_add_u32 s37, s37, s57
	s_waitcnt lgkmcnt(0)
	s_and_b32 s29, s29, 0xffff
	s_mov_b32 s30, 0x17d78400
	s_mov_b32 s31, 0x20000
	s_mov_b32 s35, 0
	s_movk_i32 s7, 0x40
	s_mov_b32 s9, 0x7fffffff
	s_lshl_b32 s44, s34, 12
	s_add_u32 s44, s44, 0x4000
	s_lshl_b32 s45, s34, 10
	s_add_u32 s45, s45, 0x8000
	s_lshl_b32 s46, s34, 4
	s_add_u32 s46, s46, 0x9000
	s_and_b32 s47, s37, 1
	s_lshl_b32 s47, s47, 2
	s_mul_i32 s38, s37, 0x9c40
	s_lshl_b32 s40, s47, 4
	s_sub_u32 s38, s38, s40
	s_add_u32 s38, s38, s43
	v_subrev_u32_e32 v8, s47, v3
	v_lshlrev_b32_e32 v8, 2, v8
	s_mul_i32 s40, s55, 0xa00
	v_add_u32_e32 v8, s40, v8
	s_mov_b64 s[48:49], -1
	s_mov_b64 s[50:51], -1
	v_mov_b32_e32 v5, v2
	v_mov_b32_e32 v6, v2
	v_mov_b32_e32 v7, v2
	s_cmp_lg_u32 s55, 0
	s_cbranch_scc1 .Lsc_i0
	s_lshl_b64 s[48:49], -1, s47
	v_max_u32_e32 v5, s47, v3
	v_lshlrev_b32_e32 v5, 4, v5
.Lsc_i0:
	s_cmp_lg_u32 s55, 3
	s_cbranch_scc1 .Lsc_i3
	s_add_i32 s41, s47, 3
	s_lshl_b64 s[50:51], 2, s41
	s_sub_u32 s50, s50, 1
	s_subb_u32 s51, s51, 0
	v_min_u32_e32 v7, s41, v3
	v_lshlrev_b32_e32 v7, 4, v7
.Lsc_i3:
	s_mul_i32 s57, s33, 0x9c40
	v_mov_b32_e32 v27, s46
	ds_read_b32 v26, v27
.Lsc_row:
	s_and_b32 s41, s35, 3
	s_lshl_b32 s40, s41, 10
	s_add_u32 s40, s40, s44
	v_mov_b32_e32 v9, s40
	s_lshl_b32 s40, s41, 8
	s_add_u32 s40, s40, s45
	v_mov_b32_e32 v10, s40
	s_lshl_b32 s40, s41, 2
	s_add_u32 s40, s40, s46
	v_mov_b32_e32 v11, s40
	s_add_u32 s39, s38, s57
	s_cmp_lt_i32 s35, s36
	s_cbranch_scc1 .Lsc_hasnext
	s_mov_b32 s39, s38
	v_mov_b32_e32 v5, 0
	v_mov_b32_e32 v6, 0
	v_mov_b32_e32 v7, 0
.Lsc_hasnext:
	s_waitcnt lgkmcnt(0)
	v_readfirstlane_b32 s42, v26
	s_cmp_eq_u32 s42, 0
	s_cbranch_scc1 .Lsc_go
.Lsc_wait:
	s_sleep 2
	ds_read_b32 v12, v11
	s_waitcnt lgkmcnt(0)
	v_readfirstlane_b32 s42, v12
	s_cmp_eq_u32 s42, 0
	s_cbranch_scc0 .Lsc_wait
.Lsc_go:
	s_add_i32 s41, s35, 1
	s_and_b32 s41, s41, 3
	s_lshl_b32 s40, s41, 2
	s_add_u32 s40, s40, s46
	v_mov_b32_e32 v27, s40
	ds_read_b32 v26, v27
	s_mov_b32 s42, 0
	s_waitcnt vmcnt(9)
	v_or3_b32 v12, v100, v101, v102
	v_bitop3_b32 v12, v12, s9, v103 bitop3:0xc8
	v_cmp_ne_u32_e32 vcc, 0, v12
	s_and_b64 vcc, vcc, s[48:49]
	s_cbranch_vccz .Lsc_s0
	s_bcnt1_i32_b64 s40, vcc
	v_mbcnt_lo_u32_b32 v13, vcc_lo, 0
	v_mbcnt_hi_u32_b32 v13, vcc_hi, v13
	v_add_u32_e32 v13, s42, v13
	s_add_i32 s42, s42, s40
	v_cmp_gt_i32_e64 s[0:1], s7, v13
	s_and_b64 s[4:5], vcc, s[0:1]
	s_and_saveexec_b64 s[0:1], s[4:5]
	v_lshl_add_u32 v14, v13, 4, v9
	v_lshl_add_u32 v15, v13, 2, v10
	v_mov_b32_e32 v13, v8
	ds_write_b128 v14, v[100:103]
	ds_write_b32 v15, v13
	s_mov_b64 exec, -1

.Lsc_s9:
	s_add_u32 s40, s39, 0x2400
	buffer_load_dwordx4 v[136:139], v7, s[28:31], s40 offen nt
	s_waitcnt lgkmcnt(0)
	s_add_i32 s42, s42, 1
	v_mov_b32_e32 v12, s42
	ds_write_b32 v11, v12
	s_cmp_eq_u32 s35, s36
	s_cbranch_scc1 .LBB1_384
	s_add_i32 s35, s35, 1
	s_mov_b32 s38, s39
	s_branch .Lsc_row
